# k_gcn: one global_load_dwordx4 for the four next neighbour indices
# speedup vs baseline: 1.0019x; 1.0019x over previous
.LBB2_9:
	v_lshl_or_b32 v34, v36, 8, v54
	buffer_load_dwordx4 v[34:37], v34, s[24:27], 0 offen
	v_lshl_or_b32 v38, v38, 8, v54
	buffer_load_dwordx4 v[38:41], v38, s[24:27], 0 offen
	v_lshl_or_b32 v42, v42, 8, v54
	buffer_load_dwordx4 v[42:45], v42, s[24:27], 0 offen
	v_lshl_or_b32 v46, v46, 8, v54
	buffer_load_dwordx4 v[46:49], v46, s[24:27], 0 offen
	v_add_lshl_u32 v68, v50, s33, 2
	v_subrev_u32_e32 v69, s33, v53
	global_load_dwordx4 v[64:67], v68, s[22:23]
.Lkg_A:
	s_waitcnt vmcnt(0)
	s_cmp_ge_i32 s33, s31
	s_cbranch_scc1 .Lkg_finA
	v_cmp_lt_i32_e64 s[34:35], 0, v69
	v_cmp_lt_i32_e64 s[36:37], 1, v69
	v_cmp_lt_i32_e64 s[38:39], 2, v69
	v_cmp_lt_i32_e64 s[40:41], 3, v69
	v_cndmask_b32_e64 v72, v70, v64, s[34:35]
	v_cndmask_b32_e64 v76, v70, v65, s[36:37]
	v_cndmask_b32_e64 v86, v70, v66, s[38:39]
	v_cndmask_b32_e64 v90, v70, v67, s[40:41]
	v_lshl_or_b32 v72, v72, 8, v54
	buffer_load_dwordx4 v[72:75], v72, s[24:27], 0 offen
	v_lshl_or_b32 v76, v76, 8, v54
	buffer_load_dwordx4 v[76:79], v76, s[24:27], 0 offen
	v_lshl_or_b32 v86, v86, 8, v54
	buffer_load_dwordx4 v[86:89], v86, s[24:27], 0 offen
	v_lshl_or_b32 v90, v90, 8, v54
	buffer_load_dwordx4 v[90:93], v90, s[24:27], 0 offen
	s_add_i32 s33, s33, 4
	v_add_lshl_u32 v68, v50, s33, 2
	v_subrev_u32_e32 v69, s33, v53
	global_load_dwordx4 v[64:67], v68, s[22:23]
	v_fma_mix_f32 v62, v34, 1.0, v62 op_sel_hi:[1,0,0]
	v_fma_mix_f32 v63, v34, 1.0, v63 op_sel:[1,0,0] op_sel_hi:[1,0,0]
	v_fma_mix_f32 v60, v35, 1.0, v60 op_sel_hi:[1,0,0]
	v_fma_mix_f32 v61, v35, 1.0, v61 op_sel:[1,0,0] op_sel_hi:[1,0,0]
	v_fma_mix_f32 v58, v36, 1.0, v58 op_sel_hi:[1,0,0]
	v_fma_mix_f32 v59, v36, 1.0, v59 op_sel:[1,0,0] op_sel_hi:[1,0,0]
	v_fma_mix_f32 v56, v37, 1.0, v56 op_sel_hi:[1,0,0]
	v_fma_mix_f32 v57, v37, 1.0, v57 op_sel:[1,0,0] op_sel_hi:[1,0,0]
	v_fma_mix_f32 v62, v38, 1.0, v62 op_sel_hi:[1,0,0]
	v_fma_mix_f32 v63, v38, 1.0, v63 op_sel:[1,0,0] op_sel_hi:[1,0,0]
	v_fma_mix_f32 v60, v39, 1.0, v60 op_sel_hi:[1,0,0]
	v_fma_mix_f32 v61, v39, 1.0, v61 op_sel:[1,0,0] op_sel_hi:[1,0,0]
	v_fma_mix_f32 v58, v40, 1.0, v58 op_sel_hi:[1,0,0]
	v_fma_mix_f32 v59, v40, 1.0, v59 op_sel:[1,0,0] op_sel_hi:[1,0,0]
	v_fma_mix_f32 v56, v41, 1.0, v56 op_sel_hi:[1,0,0]
	v_fma_mix_f32 v57, v41, 1.0, v57 op_sel:[1,0,0] op_sel_hi:[1,0,0]
	v_fma_mix_f32 v62, v42, 1.0, v62 op_sel_hi:[1,0,0]
	v_fma_mix_f32 v63, v42, 1.0, v63 op_sel:[1,0,0] op_sel_hi:[1,0,0]
	v_fma_mix_f32 v60, v43, 1.0, v60 op_sel_hi:[1,0,0]
	v_fma_mix_f32 v61, v43, 1.0, v61 op_sel:[1,0,0] op_sel_hi:[1,0,0]
	v_fma_mix_f32 v58, v44, 1.0, v58 op_sel_hi:[1,0,0]
	v_fma_mix_f32 v59, v44, 1.0, v59 op_sel:[1,0,0] op_sel_hi:[1,0,0]
	v_fma_mix_f32 v56, v45, 1.0, v56 op_sel_hi:[1,0,0]
	v_fma_mix_f32 v57, v45, 1.0, v57 op_sel:[1,0,0] op_sel_hi:[1,0,0]
	v_fma_mix_f32 v62, v46, 1.0, v62 op_sel_hi:[1,0,0]
	v_fma_mix_f32 v63, v46, 1.0, v63 op_sel:[1,0,0] op_sel_hi:[1,0,0]
	v_fma_mix_f32 v60, v47, 1.0, v60 op_sel_hi:[1,0,0]
	v_fma_mix_f32 v61, v47, 1.0, v61 op_sel:[1,0,0] op_sel_hi:[1,0,0]
	v_fma_mix_f32 v58, v48, 1.0, v58 op_sel_hi:[1,0,0]
	v_fma_mix_f32 v59, v48, 1.0, v59 op_sel:[1,0,0] op_sel_hi:[1,0,0]
	v_fma_mix_f32 v56, v49, 1.0, v56 op_sel_hi:[1,0,0]
	v_fma_mix_f32 v57, v49, 1.0, v57 op_sel:[1,0,0] op_sel_hi:[1,0,0]
.Lkg_B:
	s_waitcnt vmcnt(0)
	s_cmp_ge_i32 s33, s31
	s_cbranch_scc1 .Lkg_finB
	v_cmp_lt_i32_e64 s[34:35], 0, v69
	v_cmp_lt_i32_e64 s[36:37], 1, v69
	v_cmp_lt_i32_e64 s[38:39], 2, v69
	v_cmp_lt_i32_e64 s[40:41], 3, v69
	v_cndmask_b32_e64 v34, v70, v64, s[34:35]
	v_cndmask_b32_e64 v38, v70, v65, s[36:37]
	v_cndmask_b32_e64 v42, v70, v66, s[38:39]
	v_cndmask_b32_e64 v46, v70, v67, s[40:41]
	v_lshl_or_b32 v34, v34, 8, v54
	buffer_load_dwordx4 v[34:37], v34, s[24:27], 0 offen
	v_lshl_or_b32 v38, v38, 8, v54
	buffer_load_dwordx4 v[38:41], v38, s[24:27], 0 offen
	v_lshl_or_b32 v42, v42, 8, v54
	buffer_load_dwordx4 v[42:45], v42, s[24:27], 0 offen
	v_lshl_or_b32 v46, v46, 8, v54
	buffer_load_dwordx4 v[46:49], v46, s[24:27], 0 offen
	s_add_i32 s33, s33, 4
	v_add_lshl_u32 v68, v50, s33, 2
	v_subrev_u32_e32 v69, s33, v53
	global_load_dwordx4 v[64:67], v68, s[22:23]
	v_fma_mix_f32 v62, v72, 1.0, v62 op_sel_hi:[1,0,0]
	v_fma_mix_f32 v63, v72, 1.0, v63 op_sel:[1,0,0] op_sel_hi:[1,0,0]
	v_fma_mix_f32 v60, v73, 1.0, v60 op_sel_hi:[1,0,0]
	v_fma_mix_f32 v61, v73, 1.0, v61 op_sel:[1,0,0] op_sel_hi:[1,0,0]
	v_fma_mix_f32 v58, v74, 1.0, v58 op_sel_hi:[1,0,0]
	v_fma_mix_f32 v59, v74, 1.0, v59 op_sel:[1,0,0] op_sel_hi:[1,0,0]
	v_fma_mix_f32 v56, v75, 1.0, v56 op_sel_hi:[1,0,0]
	v_fma_mix_f32 v57, v75, 1.0, v57 op_sel:[1,0,0] op_sel_hi:[1,0,0]
	v_fma_mix_f32 v62, v76, 1.0, v62 op_sel_hi:[1,0,0]
	v_fma_mix_f32 v63, v76, 1.0, v63 op_sel:[1,0,0] op_sel_hi:[1,0,0]
	v_fma_mix_f32 v60, v77, 1.0, v60 op_sel_hi:[1,0,0]
	v_fma_mix_f32 v61, v77, 1.0, v61 op_sel:[1,0,0] op_sel_hi:[1,0,0]
	v_fma_mix_f32 v58, v78, 1.0, v58 op_sel_hi:[1,0,0]
	v_fma_mix_f32 v59, v78, 1.0, v59 op_sel:[1,0,0] op_sel_hi:[1,0,0]
	v_fma_mix_f32 v56, v79, 1.0, v56 op_sel_hi:[1,0,0]
	v_fma_mix_f32 v57, v79, 1.0, v57 op_sel:[1,0,0] op_sel_hi:[1,0,0]
	v_fma_mix_f32 v62, v86, 1.0, v62 op_sel_hi:[1,0,0]
	v_fma_mix_f32 v63, v86, 1.0, v63 op_sel:[1,0,0] op_sel_hi:[1,0,0]
	v_fma_mix_f32 v60, v87, 1.0, v60 op_sel_hi:[1,0,0]
	v_fma_mix_f32 v61, v87, 1.0, v61 op_sel:[1,0,0] op_sel_hi:[1,0,0]
	v_fma_mix_f32 v58, v88, 1.0, v58 op_sel_hi:[1,0,0]
	v_fma_mix_f32 v59, v88, 1.0, v59 op_sel:[1,0,0] op_sel_hi:[1,0,0]
	v_fma_mix_f32 v56, v89, 1.0, v56 op_sel_hi:[1,0,0]
	v_fma_mix_f32 v57, v89, 1.0, v57 op_sel:[1,0,0] op_sel_hi:[1,0,0]
	v_fma_mix_f32 v62, v90, 1.0, v62 op_sel_hi:[1,0,0]
	v_fma_mix_f32 v63, v90, 1.0, v63 op_sel:[1,0,0] op_sel_hi:[1,0,0]
	v_fma_mix_f32 v60, v91, 1.0, v60 op_sel_hi:[1,0,0]
	v_fma_mix_f32 v61, v91, 1.0, v61 op_sel:[1,0,0] op_sel_hi:[1,0,0]
	v_fma_mix_f32 v58, v92, 1.0, v58 op_sel_hi:[1,0,0]
	v_fma_mix_f32 v59, v92, 1.0, v59 op_sel:[1,0,0] op_sel_hi:[1,0,0]
	v_fma_mix_f32 v56, v93, 1.0, v56 op_sel_hi:[1,0,0]
	v_fma_mix_f32 v57, v93, 1.0, v57 op_sel:[1,0,0] op_sel_hi:[1,0,0]
	s_branch .Lkg_A
